# ho1: acquire invalidate of the panel/block hand-off waits issued before the counter poll instead of after it
# speedup vs baseline: 1.0021x; 1.0021x over previous
; __device__ __forceinline__ int fresh_lane() { unsigned m = ~0u; asm volatile("" : "+s"(m)); return (int)__builtin_amdgcn_mbcnt_hi(m, __builtin_amdgcn_mbcnt_lo(m, 0u)); }
; __device__ __forceinline__ void wg_wait_counter(const unsigned* cnt, unsigned need, unsigned* tmo, int wave) {
;     if (wave == 0) {
;         const unsigned long long t0 = __builtin_amdgcn_s_memrealtime(); unsigned polls = 0;
;         while ((unsigned)__builtin_amdgcn_readfirstlane(__hip_atomic_load(cnt, __ATOMIC_RELAXED, __HIP_MEMORY_SCOPE_AGENT)) < need) {
;             if ((++polls & 255u) == 0u && __builtin_amdgcn_readfirstlane(__hip_atomic_load(tmo, __ATOMIC_RELAXED, __HIP_MEMORY_SCOPE_AGENT)) != 0u) break;
;             if (__builtin_amdgcn_s_memrealtime() - t0 > 2000000ull) { if (fresh_lane() == 0) __hip_atomic_store(tmo, 1u, __ATOMIC_RELAXED, __HIP_MEMORY_SCOPE_AGENT); break; }
;             __builtin_amdgcn_s_sleep(2); }
;         __builtin_amdgcn_fence(__ATOMIC_ACQUIRE, "agent");
;         asm volatile("s_waitcnt vmcnt(0)" ::: "memory");
.LBB0_981:
	v_readlane_b32 s2, v252, 48
	s_add_u32 s40, s2, 0x4000
	v_readlane_b32 s2, v252, 49
	s_addc_u32 s41, s2, 0
	v_readlane_b32 s2, v253, 37
	v_readlane_b32 s3, v253, 38
	s_and_b64 vcc, exec, s[0:1]
	s_nop 0
	v_cndmask_b32_e64 v1, 0, 1, s[2:3]
	v_cmp_ne_u32_e64 s[2:3], 1, v1
	s_nop 1
	v_writelane_b32 v252, s2, 50
	s_nop 1
	v_writelane_b32 v252, s3, 51
	s_cbranch_vccnz .LBB0_1056
	v_readlane_b32 s2, v252, 50
	v_readlane_b32 s3, v252, 51
	s_and_b64 vcc, exec, s[2:3]
	s_cbranch_vccnz .LBB0_999
	v_readlane_b32 s2, v251, 16
	v_readlane_b32 s3, v251, 17
	s_and_b64 vcc, exec, s[2:3]
	s_cbranch_vccnz .LBB0_998
	s_lshl_b32 s2, s44, 6
	buffer_inv sc1
	s_memrealtime s[6:7]
	s_ashr_i32 s3, s2, 31
	s_lshl_b64 s[2:3], s[2:3], 2
	v_readlane_b32 s4, v252, 48
	s_add_u32 s4, s4, s2
	v_readlane_b32 s2, v252, 49
	s_addc_u32 s5, s2, s3
	s_mov_b32 s2, 1
	s_branch .LBB0_987

; __device__ __forceinline__ void wg_wait_counter(const unsigned* cnt, unsigned need, unsigned* tmo, int wave) {
;     ...
;         __builtin_amdgcn_fence(__ATOMIC_ACQUIRE, "agent");
;         asm volatile("s_waitcnt vmcnt(0)" ::: "memory");
.LBB0_997:
	s_waitcnt vmcnt(0) lgkmcnt(0)
	s_waitcnt vmcnt(0)

; __device__ __forceinline__ int fresh_lane() { unsigned m = ~0u; asm volatile("" : "+s"(m)); return (int)__builtin_amdgcn_mbcnt_hi(m, __builtin_amdgcn_mbcnt_lo(m, 0u)); }
; __device__ __forceinline__ void wg_wait_counter(const unsigned* cnt, unsigned need, unsigned* tmo, int wave) {
;     if (wave == 0) {
;         const unsigned long long t0 = __builtin_amdgcn_s_memrealtime(); unsigned polls = 0;
;         while ((unsigned)__builtin_amdgcn_readfirstlane(__hip_atomic_load(cnt, __ATOMIC_RELAXED, __HIP_MEMORY_SCOPE_AGENT)) < need) {
;             if ((++polls & 255u) == 0u && __builtin_amdgcn_readfirstlane(__hip_atomic_load(tmo, __ATOMIC_RELAXED, __HIP_MEMORY_SCOPE_AGENT)) != 0u) break;
;             if (__builtin_amdgcn_s_memrealtime() - t0 > 2000000ull) { if (fresh_lane() == 0) __hip_atomic_store(tmo, 1u, __ATOMIC_RELAXED, __HIP_MEMORY_SCOPE_AGENT); break; }
;             __builtin_amdgcn_s_sleep(2); }
;         __builtin_amdgcn_fence(__ATOMIC_ACQUIRE, "agent");
;         asm volatile("s_waitcnt vmcnt(0)" ::: "memory");
.LBB0_1058:
	v_readlane_b32 s2, v252, 48
	s_add_u32 s38, s2, 0x8000
	v_readlane_b32 s2, v252, 49
	s_addc_u32 s39, s2, 0
	s_and_b64 vcc, exec, s[0:1]
	s_cbranch_vccnz .LBB0_1169
	v_readlane_b32 s2, v251, 16
	v_readlane_b32 s3, v251, 17
	s_and_b64 vcc, exec, s[2:3]
	s_cbranch_vccnz .LBB0_1074
	s_lshl_b32 s2, s44, 6
	buffer_inv sc1
	s_memrealtime s[12:13]
	s_ashr_i32 s3, s2, 31
	s_lshl_b64 s[2:3], s[2:3], 2
	s_add_u32 s10, s40, s2
	s_addc_u32 s11, s41, s3
	s_mov_b32 s2, 1
	s_branch .LBB0_1063

; __device__ __forceinline__ int fresh_lane() { unsigned m = ~0u; asm volatile("" : "+s"(m)); return (int)__builtin_amdgcn_mbcnt_hi(m, __builtin_amdgcn_mbcnt_lo(m, 0u)); }
; __device__ __forceinline__ void wg_wait_counter(const unsigned* cnt, unsigned need, unsigned* tmo, int wave) {
;     if (wave == 0) {
;         const unsigned long long t0 = __builtin_amdgcn_s_memrealtime(); unsigned polls = 0;
;         while ((unsigned)__builtin_amdgcn_readfirstlane(__hip_atomic_load(cnt, __ATOMIC_RELAXED, __HIP_MEMORY_SCOPE_AGENT)) < need) {
;             if ((++polls & 255u) == 0u && __builtin_amdgcn_readfirstlane(__hip_atomic_load(tmo, __ATOMIC_RELAXED, __HIP_MEMORY_SCOPE_AGENT)) != 0u) break;
;             if (__builtin_amdgcn_s_memrealtime() - t0 > 2000000ull) { if (fresh_lane() == 0) __hip_atomic_store(tmo, 1u, __ATOMIC_RELAXED, __HIP_MEMORY_SCOPE_AGENT); break; }
;             __builtin_amdgcn_s_sleep(2); }
;         __builtin_amdgcn_fence(__ATOMIC_ACQUIRE, "agent");
;         asm volatile("s_waitcnt vmcnt(0)" ::: "memory");
.LBB0_1171:
	s_and_b64 vcc, exec, s[0:1]
	s_cbranch_vccnz .LBB0_1244
	v_readlane_b32 s0, v251, 16
	v_readlane_b32 s1, v251, 17
	v_readlane_b32 s54, v252, 16
	s_and_b64 vcc, exec, s[0:1]
	v_readlane_b32 s55, v252, 17
	s_cbranch_vccnz .LBB0_1187
	s_lshl_b32 s0, s40, 6
	buffer_inv sc1
	s_memrealtime s[4:5]
	s_ashr_i32 s1, s0, 31
	s_lshl_b64 s[0:1], s[0:1], 2
	s_add_u32 s0, s38, s0
	s_addc_u32 s1, s39, s1
	s_mov_b32 s2, 1
	s_branch .LBB0_1176

; #define LAS __attribute__((address_space(3)))
; __device__ __forceinline__ int fresh_lane() { unsigned m = ~0u; asm volatile("" : "+s"(m)); return (int)__builtin_amdgcn_mbcnt_hi(m, __builtin_amdgcn_mbcnt_lo(m, 0u)); }
; #define LDS_WAIT() asm volatile("s_waitcnt lgkmcnt(0)" ::: "memory")
; __device__ __forceinline__ void wg_wait_counter(const unsigned* cnt, unsigned need, unsigned* tmo, int wave) {
;     if (wave == 0) {
;         const unsigned long long t0 = __builtin_amdgcn_s_memrealtime(); unsigned polls = 0;
;         while ((unsigned)__builtin_amdgcn_readfirstlane(__hip_atomic_load(cnt, __ATOMIC_RELAXED, __HIP_MEMORY_SCOPE_AGENT)) < need) {
;             if ((++polls & 255u) == 0u && __builtin_amdgcn_readfirstlane(__hip_atomic_load(tmo, __ATOMIC_RELAXED, __HIP_MEMORY_SCOPE_AGENT)) != 0u) break;
;             if (__builtin_amdgcn_s_memrealtime() - t0 > 2000000ull) { if (fresh_lane() == 0) __hip_atomic_store(tmo, 1u, __ATOMIC_RELAXED, __HIP_MEMORY_SCOPE_AGENT); break; }
;             __builtin_amdgcn_s_sleep(2); }
;         __builtin_amdgcn_fence(__ATOMIC_ACQUIRE, "agent");
;         asm volatile("s_waitcnt vmcnt(0)" ::: "memory");
; __global__ void __launch_bounds__(512, 2) fwd(Args args) {
;     ...
;                 for (int j = 0; j < 12; ++j) bs[j] = *(const u32x4*)(img + (size_t)(j * 512 + tid) * 16);
; #pragma unroll
;                 for (int j = 0; j < 12; ++j) *(LAS u32x4*)(lds + (j * 512 + tid) * 16) = bs[j];
;                 LDS_WAIT();
;                 wg_wait_counter(pcnt + (3 * 64 + u.pm) * 64, 32u, ctl + CW_TMO, wave);
.LBB0_1255:
	global_load_dwordx4 v[0:3], v[24:25], off
	global_load_dwordx4 v[4:7], v[26:27], off
	global_load_dwordx4 v[8:11], v[28:29], off
	global_load_dwordx4 v[12:15], v[30:31], off
	global_load_dwordx4 v[16:19], v[32:33], off
	global_load_dwordx4 v[148:151], v[34:35], off
	global_load_dwordx4 v[152:155], v[36:37], off
	global_load_dwordx4 v[156:159], v[38:39], off
	global_load_dwordx4 v[162:165], v[40:41], off
	global_load_dwordx4 v[166:169], v[42:43], off
	global_load_dwordx4 v[170:173], v[44:45], off
	global_load_dwordx4 v[174:177], v[46:47], off
	v_readlane_b32 s0, v251, 16
	v_readlane_b32 s1, v251, 17
	s_and_b64 vcc, exec, s[0:1]
	s_waitcnt vmcnt(0)
	ds_write_b128 v97, v[0:3]
	ds_write_b128 v97, v[4:7] offset:8192
	ds_write_b128 v97, v[8:11] offset:16384
	ds_write_b128 v97, v[12:15] offset:24576
	ds_write_b128 v97, v[16:19] offset:32768
	ds_write_b128 v97, v[148:151] offset:40960
	ds_write_b128 v97, v[152:155] offset:49152
	ds_write_b128 v97, v[156:159] offset:57344
	ds_write_b128 v102, v[162:165]
	ds_write_b128 v103, v[166:169]
	ds_write_b128 v104, v[170:173]
	ds_write_b128 v105, v[174:177]
	s_waitcnt lgkmcnt(0)
	s_cbranch_vccnz .LBB0_1270
	v_readlane_b32 s0, v254, 55
	s_lshl_b32 s0, s0, 6
	s_addk_i32 s0, 0x3000
	buffer_inv sc1
	s_memrealtime s[4:5]
	s_ashr_i32 s1, s0, 31
	s_lshl_b64 s[0:1], s[0:1], 2
	v_readlane_b32 s2, v252, 48
	s_add_u32 s0, s2, s0
	v_readlane_b32 s2, v252, 49
	s_addc_u32 s1, s2, s1
	s_mov_b32 s2, 1
	s_branch .LBB0_1259

; __device__ __forceinline__ int fresh_lane() { unsigned m = ~0u; asm volatile("" : "+s"(m)); return (int)__builtin_amdgcn_mbcnt_hi(m, __builtin_amdgcn_mbcnt_lo(m, 0u)); }
;     __device__ __forceinline__ void a_ready(const pg8::Unit& u) const {
;         if (!ready) return;
;         if (wave == 0) {
;             const unsigned long long t0 = __builtin_amdgcn_s_memrealtime(); unsigned polls = 0;
;             while ((unsigned)__builtin_amdgcn_readfirstlane(__hip_atomic_load(ready + 64 * u.pm, __ATOMIC_RELAXED, __HIP_MEMORY_SCOPE_AGENT)) < need) {
;                 if ((++polls & 255u) == 0u && __builtin_amdgcn_readfirstlane(__hip_atomic_load(tmo, __ATOMIC_RELAXED, __HIP_MEMORY_SCOPE_AGENT)) != 0u) break;
;                 if (__builtin_amdgcn_s_memrealtime() - t0 > 2000000ull) { if (fresh_lane() == 0) __hip_atomic_store(tmo, 1u, __ATOMIC_RELAXED, __HIP_MEMORY_SCOPE_AGENT); break; }
;                 __builtin_amdgcn_s_sleep(2); }
;             __builtin_amdgcn_fence(__ATOMIC_ACQUIRE, "agent");
;             asm volatile("s_waitcnt vmcnt(0)" ::: "memory");
.LBB0_1525:
	s_andn2_b64 vcc, exec, s[0:1]
	s_cbranch_vccnz .LBB0_1584
	v_readlane_b32 s0, v252, 50
	v_readlane_b32 s1, v252, 51
	s_and_b64 vcc, exec, s[0:1]
	v_readlane_b32 s33, v253, 39
	s_cbranch_vccnz .LBB0_1543
	v_readlane_b32 s0, v251, 16
	v_readlane_b32 s1, v251, 17
	s_and_b64 vcc, exec, s[0:1]
	s_cbranch_vccnz .LBB0_1542
	buffer_inv sc1
	s_memrealtime s[0:1]
	s_lshl_b32 s2, s35, 6
	s_ashr_i32 s3, s2, 31
	s_lshl_b64 s[2:3], s[2:3], 2
	s_add_u32 s10, s30, s2
	s_addc_u32 s11, s31, s3
	s_mov_b32 s2, 1
	s_branch .LBB0_1531

; __device__ __forceinline__ int fresh_lane() { unsigned m = ~0u; asm volatile("" : "+s"(m)); return (int)__builtin_amdgcn_mbcnt_hi(m, __builtin_amdgcn_mbcnt_lo(m, 0u)); }
;     __device__ __forceinline__ void a_ready(const pg8::Unit& u) const { if (ready) wg_wait_counter(ready + 64 * u.pm, need, tmo, wave); }
;     __device__ __forceinline__ void a_ready(const pg8::Unit& u) const { d.a_ready(u); }
; template <class Epi, class Sched, bool GATHER, bool ALIGN_EPI>
; __device__ __forceinline__ void gemm_phase(LAS unsigned char* lds, const int wave_, const int K, const int lda, const int ldb, const Sched& S, const Epi& E) {
;     ...
;             const char* a2 = last ? nA : cA + (size_t)(t + 2) * kstep; const char* b2 = last ? nB : cB + (size_t)(t + 2) * kstep;
;             const char* a3 = a2 + kstep; const char* b3 = b2 + kstep;
;             if (last && has_next) S.a_ready(nxt);
;     __device__ __forceinline__ void a_ready(const pg8::Unit& u) const {
;         if (!ready) return;
;         if (wave == 0) {
;             const unsigned long long t0 = __builtin_amdgcn_s_memrealtime(); unsigned polls = 0;
;             while ((unsigned)__builtin_amdgcn_readfirstlane(__hip_atomic_load(ready + 64 * u.pm, __ATOMIC_RELAXED, __HIP_MEMORY_SCOPE_AGENT)) < need) {
;                 if ((++polls & 255u) == 0u && __builtin_amdgcn_readfirstlane(__hip_atomic_load(tmo, __ATOMIC_RELAXED, __HIP_MEMORY_SCOPE_AGENT)) != 0u) break;
;                 if (__builtin_amdgcn_s_memrealtime() - t0 > 2000000ull) { if (fresh_lane() == 0) __hip_atomic_store(tmo, 1u, __ATOMIC_RELAXED, __HIP_MEMORY_SCOPE_AGENT); break; }
;                 __builtin_amdgcn_s_sleep(2); }
;             __builtin_amdgcn_fence(__ATOMIC_ACQUIRE, "agent");
;             asm volatile("s_waitcnt vmcnt(0)" ::: "memory");
.LBB0_1558:
	s_cmp_lg_u32 s46, 10
	s_cselect_b64 s[20:21], -1, 0
	s_or_b64 s[2:3], s[20:21], s[16:17]
	s_and_b64 vcc, exec, s[2:3]
	s_cbranch_vccnz .LBB0_1575
	v_readlane_b32 s2, v251, 16
	v_readlane_b32 s3, v251, 17
	s_and_b64 vcc, exec, s[2:3]
	s_cbranch_vccnz .LBB0_1574
	buffer_inv sc1
	s_memrealtime s[22:23]
	s_mov_b32 s2, 1
	s_branch .LBB0_1563
